# row loops P1/P7a/P11a: next-row load waits moved to the register copies at the end of the iteration; P8 tile partial-logit A loads issued eight deep; on top of v58
# speedup vs baseline: 1.0107x; 1.0050x over previous
; __global__ void __launch_bounds__(NWAVES * 64, 2) fwd_kernel(Args a_unused) {
;     ...
;             f32x4 ca[8], cb[8];
; #pragma unroll
;             for (int j = 0; j < 8; ++j) { const int k = 4 * lane + 256 * j; const f32x4 g = *(const f32x4*)(A->norm_mix_g + k), s1 = *(const f32x4*)(modl + 2048 + k); ca[j] = g * (1.0f + s1); cb[j] = *(const f32x4*)(modl + k); }
;             f32x4 v[8], vn[8];
;             { const float* xr = A->x + (size_t)gw * D + 4 * lane;
; #pragma unroll
;               for (int j = 0; j < 8; ++j) v[j] = __builtin_nontemporal_load((const f32x4*)(xr + 256 * j)); }
;             for (int m = gw; m < NTOK; m += NGW) {
;                 if (m + NGW < NTOK) { const float* xn = A->x + (size_t)(m + NGW) * D + 4 * lane;
; #pragma unroll
;                     for (int j = 0; j < 8; ++j) vn[j] = __builtin_nontemporal_load((const f32x4*)(xn + 256 * j)); }
.LBB0_227:
	s_cmp_lt_i32 s46, 2
	s_cselect_b64 s[6:7], -1, 0
	s_lshl_b32 s95, s97, 3
	s_and_b64 s[6:7], s[6:7], s[4:5]
	s_add_i32 s58, s95, s96
	s_lshl_b32 s56, s33, 3
	v_lshl_or_b32 v166, s97, 9, v0
	s_lshl_b32 s60, s33, 9
	s_andn2_b64 vcc, exec, s[6:7]
	v_lshlrev_b32_e32 v164, 2, v162
	s_cbranch_vccnz .LBB0_248
	s_mov_b64 s[10:11], s[0:1]
	s_load_dwordx2 s[8:9], s[10:11], 0xc8
	s_ashr_i32 s59, s58, 31
	v_or_b32_e32 v1, 0x100, v164
	s_waitcnt vmcnt(11)
	v_or_b32_e32 v2, 0x200, v164
	v_or_b32_e32 v3, 0x300, v164
	v_or_b32_e32 v4, 0x400, v164
	v_or_b32_e32 v5, 0x500, v164
	s_waitcnt vmcnt(10)
	v_or_b32_e32 v6, 0x600, v164
	v_or_b32_e32 v7, 0x700, v164
	s_lshl_b64 s[12:13], s[58:59], 11
	v_mov_b32_e32 v165, 0
	s_cmpk_gt_i32 s58, 0x3fff
	s_waitcnt vmcnt(7)
	v_lshlrev_b32_e32 v98, 2, v164
	v_lshlrev_b32_e32 v140, 2, v1
	v_lshlrev_b32_e32 v141, 2, v2
	v_lshlrev_b32_e32 v139, 2, v3
	v_lshlrev_b32_e32 v138, 2, v4
	v_lshlrev_b32_e32 v137, 2, v5
	v_lshlrev_b32_e32 v136, 2, v6
	v_lshlrev_b32_e32 v1, 2, v7
	s_cbranch_scc1 .LBB0_235
	s_waitcnt lgkmcnt(0)
	s_add_u32 s4, s8, 0x100000
	s_addc_u32 s5, s9, 0
	s_add_u32 s14, s8, 0x102000
	s_addc_u32 s15, s9, 0
	global_load_dwordx4 v[34:37], v98, s[14:15]
	global_load_dwordx4 v[38:41], v140, s[14:15]
	global_load_dwordx4 v[42:45], v141, s[14:15]
	global_load_dwordx4 v[46:49], v139, s[14:15]
	global_load_dwordx4 v[50:53], v138, s[14:15]
	global_load_dwordx4 v[54:57], v137, s[14:15]
	s_load_dwordx2 s[16:17], s[10:11], 0x20
	v_mbcnt_lo_u32_b32 v2, -1, 0
	global_load_dwordx4 v[58:61], v136, s[14:15]
	global_load_dwordx4 v[62:65], v1, s[14:15]
	s_waitcnt lgkmcnt(0)
	global_load_dwordx4 v[102:105], v98, s[16:17]
	global_load_dwordx4 v[106:109], v98, s[16:17] offset:1024
	global_load_dwordx4 v[110:113], v98, s[16:17] offset:2048
	global_load_dwordx4 v[114:117], v98, s[16:17] offset:3072
	global_load_dwordx4 v[118:121], v138, s[16:17]
	global_load_dwordx4 v[122:125], v137, s[16:17]
	global_load_dwordx4 v[126:129], v136, s[16:17]
	global_load_dwordx4 v[130:133], v1, s[16:17]
	s_load_dwordx2 s[18:19], s[10:11], 0x0
	v_mbcnt_hi_u32_b32 v134, -1, v2
	v_and_b32_e32 v2, 64, v134
	s_lshl_b64 s[14:15], s[12:13], 2
	v_add_u32_e32 v146, 64, v2
	global_load_dwordx4 v[2:5], v98, s[4:5]
	global_load_dwordx4 v[6:9], v140, s[4:5]
	global_load_dwordx4 v[10:13], v141, s[4:5]
	global_load_dwordx4 v[14:17], v139, s[4:5]
	global_load_dwordx4 v[18:21], v138, s[4:5]
	global_load_dwordx4 v[22:25], v137, s[4:5]
	global_load_dwordx4 v[26:29], v136, s[4:5]
	global_load_dwordx4 v[30:33], v1, s[4:5]
	s_waitcnt lgkmcnt(0)
	s_add_u32 s4, s18, s14
	v_mov_b32_e32 v99, v165
	s_addc_u32 s5, s19, s15
	s_movk_i32 s3, 0x1000
	v_lshl_add_u64 v[66:67], s[4:5], 0, v[98:99]
	v_add_co_u32_e32 v78, vcc, s3, v66
	global_load_dwordx4 v[82:85], v98, s[4:5] offset:3072 nt
	global_load_dwordx4 v[86:89], v98, s[4:5] offset:2048 nt
	global_load_dwordx4 v[90:93], v98, s[4:5] offset:1024 nt
	global_load_dwordx4 v[94:97], v98, s[4:5] nt
	v_addc_co_u32_e32 v79, vcc, 0, v67, vcc
	global_load_dwordx4 v[66:69], v[78:79], off offset:3072 nt
	global_load_dwordx4 v[70:73], v[78:79], off offset:2048 nt
	global_load_dwordx4 v[74:77], v[78:79], off offset:1024 nt
	s_nop 0
	global_load_dwordx4 v[78:81], v[78:79], off nt
	v_xor_b32_e32 v135, 1, v134
	v_cmp_lt_i32_e32 vcc, v135, v146
	s_ashr_i32 s57, s56, 31
	s_lshl_b64 s[14:15], s[56:57], 11
	s_lshl_b64 s[16:17], s[58:59], 2
	s_add_u32 s3, s16, 0xfec000
	s_addc_u32 s24, s17, 0
	s_add_i32 s20, s58, s56
	s_ashr_i32 s21, s20, 31
	s_lshl_b64 s[16:17], s[56:57], 2
	s_lshl_b64 s[20:21], s[20:21], 13
	s_add_u32 s18, s18, s20
	s_addc_u32 s19, s19, s21
	v_cmp_eq_u32_e64 s[4:5], 0, v162
	v_mov_b32_e32 v147, 0x358637bd
	s_mov_b32 s25, 0x800000
	s_mov_b32 s26, 0x42fe0000
	s_mov_b32 s27, 0xc0c0400
	s_mov_b32 s28, 0x5040100
	s_mov_b32 s29, 0x36c00000
	s_mov_b32 s30, s58
	s_waitcnt vmcnt(25)
	v_pk_add_f32 v[60:61], v[60:61], 1.0 op_sel_hi:[1,0]
	v_pk_add_f32 v[34:35], v[34:35], 1.0 op_sel_hi:[1,0]
	v_pk_add_f32 v[36:37], v[36:37], 1.0 op_sel_hi:[1,0]
	s_waitcnt vmcnt(23)
	v_pk_mul_f32 v[102:103], v[102:103], v[34:35]
	v_cndmask_b32_e32 v34, v134, v135, vcc
	v_lshlrev_b32_e32 v99, 2, v34
	v_xor_b32_e32 v34, 2, v134
	v_cmp_lt_i32_e32 vcc, v34, v146
	v_mov_b32_e32 v35, v165
	v_pk_add_f32 v[40:41], v[40:41], 1.0 op_sel_hi:[1,0]
	v_cndmask_b32_e32 v34, v134, v34, vcc
	v_lshlrev_b32_e32 v142, 2, v34
	v_xor_b32_e32 v34, 4, v134
	v_cmp_lt_i32_e32 vcc, v34, v146
	v_pk_add_f32 v[38:39], v[38:39], 1.0 op_sel_hi:[1,0]
	v_pk_add_f32 v[44:45], v[44:45], 1.0 op_sel_hi:[1,0]
	v_cndmask_b32_e32 v34, v134, v34, vcc
	v_lshlrev_b32_e32 v143, 2, v34
	v_xor_b32_e32 v34, 8, v134
	v_cmp_lt_i32_e32 vcc, v34, v146
	v_pk_add_f32 v[42:43], v[42:43], 1.0 op_sel_hi:[1,0]
	v_pk_add_f32 v[48:49], v[48:49], 1.0 op_sel_hi:[1,0]
	v_cndmask_b32_e32 v34, v134, v34, vcc
	v_lshlrev_b32_e32 v144, 2, v34
	v_xor_b32_e32 v34, 16, v134
	v_cmp_lt_i32_e32 vcc, v34, v146
	v_pk_add_f32 v[46:47], v[46:47], 1.0 op_sel_hi:[1,0]
	v_pk_add_f32 v[52:53], v[52:53], 1.0 op_sel_hi:[1,0]
	v_cndmask_b32_e32 v34, v134, v34, vcc
	v_lshlrev_b32_e32 v145, 2, v34
	v_xor_b32_e32 v34, 32, v134
	v_cmp_lt_i32_e32 vcc, v34, v146
	v_pk_add_f32 v[50:51], v[50:51], 1.0 op_sel_hi:[1,0]
	v_pk_add_f32 v[56:57], v[56:57], 1.0 op_sel_hi:[1,0]
	v_cndmask_b32_e32 v34, v134, v34, vcc
	v_lshlrev_b32_e32 v146, 2, v34
	v_lshlrev_b32_e32 v34, 4, v162
	v_pk_add_f32 v[54:55], v[54:55], 1.0 op_sel_hi:[1,0]
	v_pk_add_f32 v[58:59], v[58:59], 1.0 op_sel_hi:[1,0]
	v_pk_add_f32 v[64:65], v[64:65], 1.0 op_sel_hi:[1,0]
	v_pk_add_f32 v[62:63], v[62:63], 1.0 op_sel_hi:[1,0]
	v_lshl_add_u64 v[34:35], s[18:19], 0, v[34:35]
	s_mov_b64 s[18:19], 0x1c00
	v_pk_mul_f32 v[100:101], v[104:105], v[36:37]
	s_waitcnt vmcnt(22)
	v_pk_mul_f32 v[104:105], v[108:109], v[40:41]
	v_pk_mul_f32 v[106:107], v[106:107], v[38:39]
	s_waitcnt vmcnt(21)
	v_pk_mul_f32 v[108:109], v[112:113], v[44:45]
	v_pk_mul_f32 v[110:111], v[110:111], v[42:43]
	s_waitcnt vmcnt(20)
	v_pk_mul_f32 v[112:113], v[116:117], v[48:49]
	v_pk_mul_f32 v[114:115], v[114:115], v[46:47]
	s_waitcnt vmcnt(19)
	v_pk_mul_f32 v[116:117], v[120:121], v[52:53]
	v_pk_mul_f32 v[118:119], v[118:119], v[50:51]
	s_waitcnt vmcnt(18)
	v_pk_mul_f32 v[120:121], v[124:125], v[56:57]
	v_pk_mul_f32 v[122:123], v[122:123], v[54:55]
	s_waitcnt vmcnt(17)
	v_pk_mul_f32 v[124:125], v[128:129], v[60:61]
	v_pk_mul_f32 v[126:127], v[126:127], v[58:59]
	s_waitcnt vmcnt(16)
	v_pk_mul_f32 v[128:129], v[132:133], v[64:65]
	v_pk_mul_f32 v[130:131], v[130:131], v[62:63]
	v_lshl_add_u64 v[132:133], s[12:13], 0, v[164:165]
	v_lshl_add_u64 v[134:135], v[34:35], 0, s[18:19]
	s_lshl_b64 s[18:19], s[56:57], 13
	s_waitcnt vmcnt(0)
	s_branch .LBB0_231
; __global__ void __launch_bounds__(NWAVES * 64, 2) fwd_kernel(Args a_unused) {
;     ...
;                 const float qi = 127.0f / am;
;                 if (lane == 0) ((float*)(ws + WS_CS + CS_HROW))[m] = am * (1.0f / 127.0f);
;                 unsigned* hq = (unsigned*)((signed char*)(ws + WS_H) + (size_t)m * D + 4 * lane);
; #pragma unroll
;                 for (int j = 0; j < 8; ++j) hq[64 * j] = q8x4(v[j][0], v[j][1], v[j][2], v[j][3], qi);
; #pragma unroll
;                 for (int j = 0; j < 8; ++j) v[j] = vn[j];
.LBB0_230:
	s_or_b64 exec, exec, s[22:23]
	v_div_scale_f32 v149, s[22:23], v148, v148, s26
	v_rcp_f32_e32 v150, v149
	v_div_scale_f32 v151, vcc, s26, v148, s26
	s_add_u32 s3, s3, s16
	v_fma_f32 v152, -v149, v150, 1.0
	v_fmac_f32_e32 v150, v152, v150
	v_mul_f32_e32 v152, v151, v150
	v_fma_f32 v153, -v149, v152, v151
	v_fmac_f32_e32 v152, v153, v150
	v_fma_f32 v149, -v149, v152, v151
	v_div_fmas_f32 v149, v149, v150, v152
	v_div_fixup_f32 v150, v149, v148, s26
	v_fmaak_f32 v96, v96, v150, 0x4b400000
	v_fmaak_f32 v97, v97, v150, 0x4b400000
	v_fmaak_f32 v94, v94, v150, 0x4b400000
	v_fmaak_f32 v95, v95, v150, 0x4b400000
	v_lshl_add_u64 v[148:149], s[8:9], 0, v[132:133]
	v_perm_b32 v94, v95, v94, s27
	v_perm_b32 v95, v97, v96, s27
	v_fmaak_f32 v92, v92, v150, 0x4b400000
	v_fmaak_f32 v93, v93, v150, 0x4b400000
	v_fmaak_f32 v90, v90, v150, 0x4b400000
	v_fmaak_f32 v91, v91, v150, 0x4b400000
	v_fmaak_f32 v88, v88, v150, 0x4b400000
	v_fmaak_f32 v89, v89, v150, 0x4b400000
	v_fmaak_f32 v86, v86, v150, 0x4b400000
	v_fmaak_f32 v87, v87, v150, 0x4b400000
	v_fmaak_f32 v84, v84, v150, 0x4b400000
	v_fmaak_f32 v85, v85, v150, 0x4b400000
	v_fmaak_f32 v82, v82, v150, 0x4b400000
	v_fmaak_f32 v83, v83, v150, 0x4b400000
	v_fmaak_f32 v80, v80, v150, 0x4b400000
	v_fmaak_f32 v81, v81, v150, 0x4b400000
	v_fmaak_f32 v78, v78, v150, 0x4b400000
	v_fmaak_f32 v79, v79, v150, 0x4b400000
	v_fmaak_f32 v76, v76, v150, 0x4b400000
	v_fmaak_f32 v77, v77, v150, 0x4b400000
	v_fmaak_f32 v74, v74, v150, 0x4b400000
	v_fmaak_f32 v75, v75, v150, 0x4b400000
	v_fmaak_f32 v72, v72, v150, 0x4b400000
	v_fmaak_f32 v73, v73, v150, 0x4b400000
	v_fmaak_f32 v70, v70, v150, 0x4b400000
	v_fmaak_f32 v71, v71, v150, 0x4b400000
	v_fmaak_f32 v68, v68, v150, 0x4b400000
	v_fmaak_f32 v69, v69, v150, 0x4b400000
	v_fmaak_f32 v66, v66, v150, 0x4b400000
	v_fmaak_f32 v67, v67, v150, 0x4b400000
	v_perm_b32 v96, v94, v95, s28
	v_add_co_u32_e32 v94, vcc, s29, v148
	v_perm_b32 v90, v91, v90, s27
	v_perm_b32 v91, v93, v92, s27
	v_perm_b32 v86, v87, v86, s27
	v_perm_b32 v87, v89, v88, s27
	v_perm_b32 v82, v83, v82, s27
	v_perm_b32 v83, v85, v84, s27
	v_perm_b32 v78, v79, v78, s27
	v_perm_b32 v79, v81, v80, s27
	v_perm_b32 v74, v75, v74, s27
	v_perm_b32 v75, v77, v76, s27
	v_perm_b32 v70, v71, v70, s27
	v_perm_b32 v71, v73, v72, s27
	v_perm_b32 v66, v67, v66, s27
	v_perm_b32 v67, v69, v68, s27
	v_addc_co_u32_e32 v95, vcc, 0, v149, vcc
	v_perm_b32 v90, v90, v91, s28
	v_perm_b32 v86, v86, v87, s28
	v_perm_b32 v82, v82, v83, s28
	v_perm_b32 v78, v78, v79, s28
	v_perm_b32 v74, v74, v75, s28
	v_perm_b32 v70, v70, v71, s28
	v_perm_b32 v66, v66, v67, s28
	global_store_dword v[94:95], v96, off
	global_store_dword v[94:95], v90, off offset:256
	global_store_dword v[94:95], v86, off offset:512
	global_store_dword v[94:95], v82, off offset:768
	global_store_dword v[94:95], v78, off offset:1024
	global_store_dword v[94:95], v74, off offset:1280
	global_store_dword v[94:95], v70, off offset:1536
	global_store_dword v[94:95], v66, off offset:1792
	s_waitcnt vmcnt(8)
	v_mov_b64_e32 v[96:97], v[36:37]
	v_mov_b64_e32 v[92:93], v[40:41]
	v_mov_b64_e32 v[88:89], v[44:45]
	v_mov_b64_e32 v[84:85], v[48:49]
	v_mov_b64_e32 v[80:81], v[52:53]
	v_mov_b64_e32 v[76:77], v[56:57]
	v_mov_b64_e32 v[72:73], v[60:61]
	v_mov_b64_e32 v[68:69], v[64:65]
	v_lshl_add_u64 v[132:133], v[132:133], 0, s[14:15]
	s_addc_u32 s24, s24, s17
	v_lshl_add_u64 v[134:135], v[134:135], 0, s[18:19]
	s_and_b64 vcc, exec, s[20:21]
	v_mov_b64_e32 v[94:95], v[34:35]
	v_mov_b64_e32 v[90:91], v[38:39]
	v_mov_b64_e32 v[86:87], v[42:43]
	v_mov_b64_e32 v[82:83], v[46:47]
	v_mov_b64_e32 v[78:79], v[50:51]
	v_mov_b64_e32 v[74:75], v[54:55]
	v_mov_b64_e32 v[70:71], v[58:59]
	v_mov_b64_e32 v[66:67], v[62:63]
	s_cbranch_vccnz .LBB0_235

; __global__ void __launch_bounds__(NWAVES * 64, 2) fwd_kernel(Args a_unused) {
;     ...
;                 float ss = 0.f;
; #pragma unroll
;                 for (int j = 0; j < 8; ++j) ss += v[j][0] * v[j][0] + v[j][1] * v[j][1] + v[j][2] * v[j][2] + v[j][3] * v[j][3];
;                 const float rstd = rsqrtf(wave_sum(ss) * (1.0f / D) + EPS);
;                 float am = 0.f;
; #pragma unroll
;                 for (int j = 0; j < 8; ++j) { v[j] = v[j] * rstd * ca[j] + cb[j]; am = fmaxf(am, fmaxf(fmaxf(fabsf(v[j][0]), fabsf(v[j][1])), fmaxf(fabsf(v[j][2]), fabsf(v[j][3])))); }
; #pragma unroll
;                 for (int o = 1; o < 64; o <<= 1) am = fmaxf(am, __shfl_xor(am, o));
;                 if (am == 0.f) am = 1.f;
;                 const float qi = 127.0f / am;
;                 if (lane == 0) ((float*)(ws + WS_CS + CS_HROW))[m] = am * (1.0f / 127.0f);
.LBB0_233:
	v_mul_f32_e32 v148, v95, v95
	v_mul_f32_e32 v149, v91, v91
	v_fmac_f32_e32 v148, v94, v94
	v_fmac_f32_e32 v149, v90, v90
	v_fmac_f32_e32 v148, v96, v96
	v_fmac_f32_e32 v149, v92, v92
	v_fmac_f32_e32 v148, v97, v97
	v_fmac_f32_e32 v149, v93, v93
	v_add_f32_e32 v148, v148, v149
	v_mul_f32_e32 v149, v87, v87
	v_fmac_f32_e32 v149, v86, v86
	v_fmac_f32_e32 v149, v88, v88
	v_fmac_f32_e32 v149, v89, v89
	v_add_f32_e32 v148, v148, v149
	v_mul_f32_e32 v149, v83, v83
	v_fmac_f32_e32 v149, v82, v82
	v_fmac_f32_e32 v149, v84, v84
	v_fmac_f32_e32 v149, v85, v85
	v_mov_b32_e32 v150, v79
	v_mov_b32_e32 v151, v75
	v_add_f32_e32 v152, v148, v149
	v_mov_b32_e32 v148, v78
	v_mov_b32_e32 v149, v74
	v_pk_mul_f32 v[150:151], v[150:151], v[150:151]
	s_nop 0
	v_pk_fma_f32 v[148:149], v[148:149], v[148:149], v[150:151]
	v_mov_b32_e32 v150, v80
	v_mov_b32_e32 v151, v76
	v_pk_fma_f32 v[148:149], v[150:151], v[150:151], v[148:149]
	v_mov_b32_e32 v150, v81
	v_mov_b32_e32 v151, v77
	v_pk_fma_f32 v[148:149], v[150:151], v[150:151], v[148:149]
	v_mov_b32_e32 v150, v71
	v_add_f32_e32 v148, v152, v148
	v_mov_b32_e32 v151, v67
	v_add_f32_e32 v152, v148, v149
	v_mov_b32_e32 v148, v70
	v_mov_b32_e32 v149, v66
	v_pk_mul_f32 v[150:151], v[150:151], v[150:151]
	s_nop 0
	v_pk_fma_f32 v[148:149], v[148:149], v[148:149], v[150:151]
	v_mov_b32_e32 v150, v72
	v_mov_b32_e32 v151, v68
	v_pk_fma_f32 v[148:149], v[150:151], v[150:151], v[148:149]
	v_mov_b32_e32 v150, v73
	v_mov_b32_e32 v151, v69
	v_pk_fma_f32 v[148:149], v[150:151], v[150:151], v[148:149]
	s_nop 0
	v_add_f32_e32 v148, v152, v148
	v_add_f32_e32 v148, v148, v149
	s_waitcnt lgkmcnt(0)
	s_nop 1
	v_add_f32_dpp v148, v148, v148 quad_perm:[1,0,3,2] row_mask:0xf bank_mask:0xf
	s_nop 1
	v_add_f32_dpp v148, v148, v148 quad_perm:[2,3,0,1] row_mask:0xf bank_mask:0xf
	s_nop 1
	v_add_f32_dpp v148, v148, v148 row_half_mirror row_mask:0xf bank_mask:0xf
	s_nop 1
	v_add_f32_dpp v148, v148, v148 row_mirror row_mask:0xf bank_mask:0xf
	v_mov_b32_e32 v149, v148
	s_nop 1
	v_permlane16_swap_b32 v148, v149
	v_add_f32_e32 v148, v148, v149
	v_mov_b32_e32 v149, v148
	s_nop 1
	v_permlane32_swap_b32 v148, v149
	v_add_f32_e32 v148, v148, v149
	v_fmamk_f32 v148, v148, 0x3a000000, v147
	v_mul_f32_e32 v149, 0x4b800000, v148
	v_cmp_gt_f32_e32 vcc, s25, v148
	s_nop 1
	v_cndmask_b32_e32 v148, v148, v149, vcc
	v_rsq_f32_e32 v148, v148
	s_nop 0
	v_mul_f32_e32 v149, 0x45800000, v148
	v_cndmask_b32_e32 v148, v148, v149, vcc
	v_pk_mul_f32 v[150:151], v[148:149], v[94:95] op_sel_hi:[0,1]
	v_pk_mul_f32 v[94:95], v[148:149], v[96:97] op_sel_hi:[0,1]
	v_pk_fma_f32 v[94:95], v[94:95], v[100:101], v[4:5]
	v_pk_fma_f32 v[96:97], v[150:151], v[102:103], v[2:3]
	v_max_f32_e64 v149, |v94|, |v95|
	v_max3_f32 v149, |v96|, |v97|, v149
	v_pk_mul_f32 v[150:151], v[148:149], v[90:91] op_sel_hi:[0,1]
	v_pk_mul_f32 v[90:91], v[148:149], v[92:93] op_sel_hi:[0,1]
	v_pk_fma_f32 v[90:91], v[90:91], v[104:105], v[8:9]
	v_pk_fma_f32 v[92:93], v[150:151], v[106:107], v[6:7]
	v_max_f32_e64 v150, |v90|, |v91|
	v_max3_f32 v150, |v92|, |v93|, v150
	v_max3_f32 v149, v149, 0, v150
	v_pk_mul_f32 v[150:151], v[148:149], v[86:87] op_sel_hi:[0,1]
	v_pk_mul_f32 v[86:87], v[148:149], v[88:89] op_sel_hi:[0,1]
	v_pk_fma_f32 v[86:87], v[86:87], v[108:109], v[12:13]
	v_pk_fma_f32 v[88:89], v[150:151], v[110:111], v[10:11]
	v_max_f32_e64 v150, |v86|, |v87|
	v_max3_f32 v152, |v88|, |v89|, v150
	v_pk_mul_f32 v[150:151], v[148:149], v[82:83] op_sel_hi:[0,1]
	v_pk_mul_f32 v[82:83], v[148:149], v[84:85] op_sel_hi:[0,1]
	v_pk_fma_f32 v[82:83], v[82:83], v[112:113], v[16:17]
	v_pk_fma_f32 v[84:85], v[150:151], v[114:115], v[14:15]
	v_max_f32_e64 v150, |v82|, |v83|
	v_max3_f32 v150, |v84|, |v85|, v150
	v_max3_f32 v149, v149, v152, v150
	v_pk_mul_f32 v[150:151], v[148:149], v[78:79] op_sel_hi:[0,1]
	v_pk_mul_f32 v[78:79], v[148:149], v[80:81] op_sel_hi:[0,1]
	v_pk_fma_f32 v[78:79], v[78:79], v[116:117], v[20:21]
	v_pk_fma_f32 v[80:81], v[150:151], v[118:119], v[18:19]
	v_max_f32_e64 v150, |v78|, |v79|
	v_max3_f32 v152, |v80|, |v81|, v150
	v_pk_mul_f32 v[150:151], v[148:149], v[74:75] op_sel_hi:[0,1]
	v_pk_mul_f32 v[74:75], v[148:149], v[76:77] op_sel_hi:[0,1]
	v_pk_fma_f32 v[74:75], v[74:75], v[120:121], v[24:25]
	v_pk_fma_f32 v[76:77], v[150:151], v[122:123], v[22:23]
	v_max_f32_e64 v150, |v74|, |v75|
	v_max3_f32 v150, |v76|, |v77|, v150
	v_max3_f32 v149, v149, v152, v150
	v_pk_mul_f32 v[150:151], v[148:149], v[70:71] op_sel_hi:[0,1]
	v_pk_mul_f32 v[70:71], v[148:149], v[72:73] op_sel_hi:[0,1]
	v_pk_fma_f32 v[70:71], v[70:71], v[124:125], v[28:29]
	v_pk_fma_f32 v[72:73], v[150:151], v[126:127], v[26:27]
	v_max_f32_e64 v150, |v70|, |v71|
	v_max3_f32 v152, |v72|, |v73|, v150
	v_pk_mul_f32 v[150:151], v[148:149], v[66:67] op_sel_hi:[0,1]
	v_pk_mul_f32 v[66:67], v[148:149], v[68:69] op_sel_hi:[0,1]
	v_pk_fma_f32 v[66:67], v[66:67], v[128:129], v[32:33]
	v_pk_fma_f32 v[68:69], v[150:151], v[130:131], v[30:31]
	v_max_f32_e64 v148, |v66|, |v67|
	v_max3_f32 v148, |v68|, |v69|, v148
	v_max3_f32 v148, v149, v152, v148
	s_waitcnt lgkmcnt(0)
	s_nop 1
	v_max_f32_dpp v148, v148, v148 quad_perm:[1,0,3,2] row_mask:0xf bank_mask:0xf
	s_nop 1
	v_max_f32_dpp v148, v148, v148 quad_perm:[2,3,0,1] row_mask:0xf bank_mask:0xf
	s_nop 1
	v_max_f32_dpp v148, v148, v148 row_half_mirror row_mask:0xf bank_mask:0xf
	s_nop 1
	v_max_f32_dpp v148, v148, v148 row_mirror row_mask:0xf bank_mask:0xf
	v_mov_b32_e32 v149, v148
	s_nop 1
	v_permlane16_swap_b32 v148, v149
	v_max_f32_e32 v148, v148, v149
	v_mov_b32_e32 v149, v148
	s_nop 1
	v_permlane32_swap_b32 v148, v149
	v_max_f32_e32 v148, v148, v149
	v_cmp_neq_f32_e32 vcc, 0, v148
	s_nop 1
	v_cndmask_b32_e32 v148, 1.0, v148, vcc
	s_and_saveexec_b64 s[22:23], s[4:5]
	s_cbranch_execz .LBB0_230
	s_add_u32 s34, s8, s3
	s_addc_u32 s35, s9, s24
	v_mul_f32_e32 v149, 0x3c010204, v148
	global_store_dword v165, v149, s[34:35]
	s_branch .LBB0_230

; DI float bflo(unsigned w) { return __uint_as_float(w << 16); }
; DI float bfhi(unsigned w) { return __uint_as_float(w & 0xffff0000u); }
; __global__ void __launch_bounds__(NWAVES * 64, 2) fwd_kernel(Args a_unused) {
;     ...
;         { u32x2 v[8], vn[8]; const unsigned short* MB = (const unsigned short*)(ws + WS_MERGED);
;           if (gw < NTOK) { const unsigned short* ar = MB + (size_t)gw * D + 4 * lane;
; #pragma unroll
;               for (int j = 0; j < 8; ++j) v[j] = *(const u32x2*)(ar + 256 * j); }
;           for (int m = gw; m < NTOK; m += NGW) {
;               if (m + NGW < NTOK) { const unsigned short* an = MB + (size_t)(m + NGW) * D + 4 * lane;
; #pragma unroll
;                   for (int j = 0; j < 8; ++j) vn[j] = *(const u32x2*)(an + 256 * j); }
;               float am = 0.f;
; #pragma unroll
;               for (int j = 0; j < 8; ++j) am = fmaxf(am, fmaxf(fmaxf(fabsf(bflo(v[j][0])), fabsf(bfhi(v[j][0]))), fmaxf(fabsf(bflo(v[j][1])), fabsf(bfhi(v[j][1])))));
; #pragma unroll
;               for (int o = 1; o < 64; o <<= 1) am = fmaxf(am, __shfl_xor(am, o));
;               if (!(am > 0.f)) am = 1.f;
;               const float qi = 127.0f / am;
;               if (lane == 0) ((float*)(ws + WS_DLOG + DL_MRS))[m] = am * (1.0f / 127.0f);
;               unsigned* aq = (unsigned*)((signed char*)(ws + WS_YAB) + (size_t)m * D + 4 * lane);
; #pragma unroll
;               for (int j = 0; j < 8; ++j) { const unsigned b0 = __float_as_uint(__builtin_fmaf(bflo(v[j][0]), qi, 12582912.0f)), b1 = __float_as_uint(__builtin_fmaf(bfhi(v[j][0]), qi, 12582912.0f)),
;                                                            b2 = __float_as_uint(__builtin_fmaf(bflo(v[j][1]), qi, 12582912.0f)), b3 = __float_as_uint(__builtin_fmaf(bfhi(v[j][1]), qi, 12582912.0f));
;                   aq[64 * j] = __builtin_amdgcn_perm(__builtin_amdgcn_perm(b3, b2, 0x0c0c0400u), __builtin_amdgcn_perm(b1, b0, 0x0c0c0400u), 0x05040100u); }
; #pragma unroll
;               for (int j = 0; j < 8; ++j) v[j] = vn[j];
.LBB0_1555:
	s_cmp_lt_i32 s46, 8
	s_cselect_b64 s[6:7], -1, 0
	s_and_b64 s[6:7], s[6:7], s[4:5]
	s_andn2_b64 vcc, exec, s[6:7]
	s_cbranch_vccnz .LBB0_1662
	v_readlane_b32 s10, v254, 6
	v_readlane_b32 s11, v254, 7
	s_waitcnt lgkmcnt(0)
	s_load_dwordx2 s[8:9], s[10:11], 0xc8
	s_cmpk_gt_i32 s58, 0x3fff
	s_cbranch_scc1 .LBB0_1563
	s_ashr_i32 s59, s58, 31
	s_lshl_b64 s[4:5], s[58:59], 12
	s_waitcnt lgkmcnt(0)
	s_add_u32 s4, s8, s4
	s_addc_u32 s5, s9, s5
	s_waitcnt vmcnt(0)
	v_lshlrev_b32_e32 v2, 3, v162
	v_mov_b32_e32 v3, 0
	v_lshl_add_u64 v[4:5], s[4:5], 0, v[2:3]
	s_mov_b64 s[4:5], 0x5bc00000
	v_lshl_add_u64 v[6:7], v[4:5], 0, s[4:5]
	v_add_co_u32_e32 v4, vcc, 0x5bc00000, v4
	v_mbcnt_lo_u32_b32 v1, -1, 0
	s_nop 0
	v_addc_co_u32_e32 v5, vcc, 0, v5, vcc
	global_load_dwordx2 v[36:37], v[6:7], off offset:512
	global_load_dwordx2 v[34:35], v[6:7], off offset:1024
	global_load_dwordx2 v[32:33], v[6:7], off offset:1536
	global_load_dwordx2 v[30:31], v[6:7], off offset:2048
	global_load_dwordx2 v[38:39], v[4:5], off
	global_load_dwordx2 v[28:29], v[6:7], off offset:2560
	global_load_dwordx2 v[26:27], v[6:7], off offset:3072
	global_load_dwordx2 v[24:25], v[6:7], off offset:3584
	v_mbcnt_hi_u32_b32 v4, -1, v1
	v_and_b32_e32 v1, 64, v4
	v_add_u32_e32 v5, 64, v1
	v_xor_b32_e32 v1, 1, v4
	v_cmp_lt_i32_e32 vcc, v1, v5
	v_xor_b32_e32 v2, 2, v4
	v_xor_b32_e32 v6, 4, v4
	v_cndmask_b32_e32 v1, v4, v1, vcc
	v_cmp_lt_i32_e32 vcc, v2, v5
	s_lshl_b64 s[12:13], s[58:59], 11
	s_ashr_i32 s57, s56, 31
	v_cndmask_b32_e32 v2, v4, v2, vcc
	v_cmp_lt_i32_e32 vcc, v6, v5
	s_lshl_b64 s[14:15], s[58:59], 2
	v_cmp_eq_u32_e64 s[4:5], 0, v162
	v_cndmask_b32_e32 v6, v4, v6, vcc
	v_lshlrev_b32_e32 v40, 2, v6
	v_xor_b32_e32 v6, 8, v4
	v_cmp_lt_i32_e32 vcc, v6, v5
	v_lshlrev_b32_e32 v1, 2, v1
	v_lshlrev_b32_e32 v2, 2, v2
	v_cndmask_b32_e32 v6, v4, v6, vcc
	v_lshlrev_b32_e32 v41, 2, v6
	v_xor_b32_e32 v6, 16, v4
	v_cmp_lt_i32_e32 vcc, v6, v5
	s_mov_b32 s23, 0x42fe0000
	s_mov_b32 s24, 0xc0c0400
	v_cndmask_b32_e32 v6, v4, v6, vcc
	v_lshlrev_b32_e32 v42, 2, v6
	v_xor_b32_e32 v6, 32, v4
	v_cmp_lt_i32_e32 vcc, v6, v5
	v_mov_b32_e32 v5, s13
	s_mov_b32 s25, 0x5040100
	v_cndmask_b32_e32 v4, v4, v6, vcc
	v_lshlrev_b32_e32 v43, 2, v4
	v_lshl_or_b32 v4, v162, 2, s12
	s_lshl_b64 s[12:13], s[56:57], 11
	s_add_u32 s3, s14, 0x4c2000
	s_addc_u32 s22, s15, 0
	s_add_i32 s16, s58, s56
	s_ashr_i32 s17, s16, 31
	s_lshl_b64 s[16:17], s[16:17], 12
	s_lshl_b64 s[14:15], s[56:57], 2
	v_lshl_or_b32 v6, v162, 3, s16
	v_mov_b32_e32 v7, s17
	s_lshl_b64 s[16:17], s[56:57], 12
	s_mov_b32 s26, 0x4fc00000
	s_mov_b32 s27, s58
	s_waitcnt vmcnt(0)
	s_branch .LBB0_1559
.LBB0_1558:
	s_or_b64 exec, exec, s[20:21]
	v_div_scale_f32 v61, s[20:21], v60, v60, s23
	v_rcp_f32_e32 v62, v61
	v_div_scale_f32 v63, vcc, s23, v60, s23
	s_add_u32 s3, s3, s14
	v_fma_f32 v64, -v61, v62, 1.0
	v_fmac_f32_e32 v62, v64, v62
	v_mul_f32_e32 v64, v63, v62
	v_fma_f32 v65, -v61, v64, v63
	v_fmac_f32_e32 v64, v65, v62
	v_fma_f32 v61, -v61, v64, v63
	v_div_fmas_f32 v61, v61, v62, v64
	v_div_fixup_f32 v62, v61, v60, s23
	v_fmaak_f32 v56, v56, v62, 0x4b400000
	v_fmaak_f32 v57, v57, v62, 0x4b400000
	v_fmaak_f32 v58, v58, v62, 0x4b400000
	v_fmaak_f32 v59, v59, v62, 0x4b400000
	v_lshl_add_u64 v[60:61], s[8:9], 0, v[4:5]
	v_perm_b32 v58, v59, v58, s24
	v_perm_b32 v56, v57, v56, s24
	v_fmaak_f32 v38, v38, v62, 0x4b400000
	v_fmaak_f32 v36, v36, v62, 0x4b400000
	v_fmaak_f32 v39, v39, v62, 0x4b400000
	v_fmaak_f32 v37, v37, v62, 0x4b400000
	v_perm_b32 v58, v58, v56, s25
	v_add_co_u32_e32 v56, vcc, s26, v60
	v_perm_b32 v37, v37, v39, s24
	v_perm_b32 v36, v36, v38, s24
	v_addc_co_u32_e32 v57, vcc, 0, v61, vcc
	v_perm_b32 v36, v37, v36, s25
	global_store_dword v[56:57], v36, off offset:256
	v_fmaak_f32 v36, v44, v62, 0x4b400000
	v_fmaak_f32 v34, v34, v62, 0x4b400000
	v_fmaak_f32 v37, v45, v62, 0x4b400000
	v_fmaak_f32 v35, v35, v62, 0x4b400000
	v_perm_b32 v35, v35, v37, s24
	v_perm_b32 v34, v34, v36, s24
	v_perm_b32 v34, v35, v34, s25
	global_store_dword v[56:57], v34, off offset:512
	v_fmaak_f32 v34, v46, v62, 0x4b400000
	v_fmaak_f32 v32, v32, v62, 0x4b400000
	v_fmaak_f32 v35, v47, v62, 0x4b400000
	v_fmaak_f32 v33, v33, v62, 0x4b400000
	v_perm_b32 v33, v33, v35, s24
	v_perm_b32 v32, v32, v34, s24
	v_perm_b32 v32, v33, v32, s25
	global_store_dword v[56:57], v32, off offset:768
	v_fmaak_f32 v32, v48, v62, 0x4b400000
	v_fmaak_f32 v30, v30, v62, 0x4b400000
	v_fmaak_f32 v33, v49, v62, 0x4b400000
	v_fmaak_f32 v31, v31, v62, 0x4b400000
	v_perm_b32 v31, v31, v33, s24
	v_perm_b32 v30, v30, v32, s24
	v_perm_b32 v30, v31, v30, s25
	global_store_dword v[56:57], v30, off offset:1024
	v_fmaak_f32 v30, v50, v62, 0x4b400000
	v_fmaak_f32 v28, v28, v62, 0x4b400000
	v_fmaak_f32 v31, v51, v62, 0x4b400000
	v_fmaak_f32 v29, v29, v62, 0x4b400000
	v_perm_b32 v29, v29, v31, s24
	v_perm_b32 v28, v28, v30, s24
	v_perm_b32 v28, v29, v28, s25
	global_store_dword v[56:57], v28, off offset:1280
	v_fmaak_f32 v28, v52, v62, 0x4b400000
	v_fmaak_f32 v26, v26, v62, 0x4b400000
	v_fmaak_f32 v29, v53, v62, 0x4b400000
	v_fmaak_f32 v27, v27, v62, 0x4b400000
	v_perm_b32 v27, v27, v29, s24
	v_perm_b32 v26, v26, v28, s24
	v_perm_b32 v26, v27, v26, s25
	global_store_dword v[56:57], v26, off offset:1536
	v_fmaak_f32 v26, v54, v62, 0x4b400000
	v_fmaak_f32 v24, v24, v62, 0x4b400000
	v_fmaak_f32 v27, v55, v62, 0x4b400000
	v_fmaak_f32 v25, v25, v62, 0x4b400000
	v_perm_b32 v25, v25, v27, s24
	v_perm_b32 v24, v24, v26, s24
	v_perm_b32 v24, v25, v24, s25
	global_store_dword v[56:57], v24, off offset:1792
	v_lshl_add_u64 v[4:5], v[4:5], 0, s[12:13]
	s_addc_u32 s22, s22, s15
	v_lshl_add_u64 v[6:7], v[6:7], 0, s[16:17]
	s_and_b64 vcc, exec, s[18:19]
	s_waitcnt vmcnt(7)
	v_mov_b64_e32 v[38:39], v[8:9]
	v_mov_b64_e32 v[36:37], v[10:11]
	v_mov_b64_e32 v[34:35], v[12:13]
	v_mov_b64_e32 v[32:33], v[14:15]
	v_mov_b64_e32 v[30:31], v[16:17]
	v_mov_b64_e32 v[28:29], v[18:19]
	v_mov_b64_e32 v[26:27], v[20:21]
	v_mov_b64_e32 v[24:25], v[22:23]
	global_store_dword v[56:57], v58, off
	s_cbranch_vccnz .LBB0_1563

; DI float bflo(unsigned w) { return __uint_as_float(w << 16); }
; DI float bfhi(unsigned w) { return __uint_as_float(w & 0xffff0000u); }
; __global__ void __launch_bounds__(NWAVES * 64, 2) fwd_kernel(Args a_unused) {
;     ...
;               float am = 0.f;
; #pragma unroll
;               for (int j = 0; j < 8; ++j) am = fmaxf(am, fmaxf(fmaxf(fabsf(bflo(v[j][0])), fabsf(bfhi(v[j][0]))), fmaxf(fabsf(bflo(v[j][1])), fabsf(bfhi(v[j][1])))));
; #pragma unroll
;               for (int o = 1; o < 64; o <<= 1) am = fmaxf(am, __shfl_xor(am, o));
;               if (!(am > 0.f)) am = 1.f;
;               const float qi = 127.0f / am;
;               if (lane == 0) ((float*)(ws + WS_DLOG + DL_MRS))[m] = am * (1.0f / 127.0f);
.LBB0_1561:
	v_lshlrev_b32_e32 v58, 16, v39
	v_and_b32_e32 v59, 0xffff0000, v39
	v_lshlrev_b32_e32 v56, 16, v38
	v_and_b32_e32 v57, 0xffff0000, v38
	v_max_f32_e64 v38, |v59|, |v59|
	v_max_f32_e64 v39, |v58|, |v58|
	v_max_f32_e32 v38, v39, v38
	v_lshlrev_b32_e32 v39, 16, v37
	v_and_b32_e32 v37, 0xffff0000, v37
	v_max_f32_e64 v45, |v37|, |v37|
	v_max_f32_e64 v46, |v39|, |v39|
	v_max3_f32 v44, |v56|, |v57|, v38
	v_lshlrev_b32_e32 v38, 16, v36
	v_and_b32_e32 v36, 0xffff0000, v36
	v_max_f32_e32 v45, v46, v45
	v_max3_f32 v45, |v38|, |v36|, v45
	v_max3_f32 v48, v44, 0, v45
	v_lshlrev_b32_e32 v45, 16, v35
	v_and_b32_e32 v35, 0xffff0000, v35
	v_max_f32_e64 v46, |v35|, |v35|
	v_max_f32_e64 v47, |v45|, |v45|
	v_max_f32_e32 v46, v47, v46
	v_lshlrev_b32_e32 v47, 16, v33
	v_and_b32_e32 v33, 0xffff0000, v33
	v_lshlrev_b32_e32 v44, 16, v34
	v_and_b32_e32 v34, 0xffff0000, v34
	v_max_f32_e64 v50, |v33|, |v33|
	v_max_f32_e64 v51, |v47|, |v47|
	v_max3_f32 v49, |v44|, |v34|, v46
	v_lshlrev_b32_e32 v46, 16, v32
	v_and_b32_e32 v32, 0xffff0000, v32
	v_max_f32_e32 v50, v51, v50
	v_max3_f32 v50, |v46|, |v32|, v50
	v_max3_f32 v52, v48, v49, v50
	v_lshlrev_b32_e32 v49, 16, v31
	v_and_b32_e32 v31, 0xffff0000, v31
	v_max_f32_e64 v50, |v31|, |v31|
	v_max_f32_e64 v51, |v49|, |v49|
	v_max_f32_e32 v50, v51, v50
	v_lshlrev_b32_e32 v51, 16, v29
	v_and_b32_e32 v29, 0xffff0000, v29
	v_lshlrev_b32_e32 v48, 16, v30
	v_and_b32_e32 v30, 0xffff0000, v30
	v_max_f32_e64 v54, |v29|, |v29|
	v_max_f32_e64 v55, |v51|, |v51|
	v_max3_f32 v53, |v48|, |v30|, v50
	v_lshlrev_b32_e32 v50, 16, v28
	v_and_b32_e32 v28, 0xffff0000, v28
	v_max_f32_e32 v54, v55, v54
	v_max3_f32 v54, |v50|, |v28|, v54
	v_max3_f32 v60, v52, v53, v54
	v_lshlrev_b32_e32 v53, 16, v27
	v_and_b32_e32 v27, 0xffff0000, v27
	v_max_f32_e64 v54, |v27|, |v27|
	v_max_f32_e64 v55, |v53|, |v53|
	v_max_f32_e32 v54, v55, v54
	v_lshlrev_b32_e32 v55, 16, v25
	v_and_b32_e32 v25, 0xffff0000, v25
	v_lshlrev_b32_e32 v52, 16, v26
	v_and_b32_e32 v26, 0xffff0000, v26
	v_max_f32_e64 v62, |v25|, |v25|
	v_max_f32_e64 v63, |v55|, |v55|
	v_max3_f32 v61, |v52|, |v26|, v54
	v_lshlrev_b32_e32 v54, 16, v24
	v_and_b32_e32 v24, 0xffff0000, v24
	v_max_f32_e32 v62, v63, v62
	v_max3_f32 v62, |v54|, |v24|, v62
	v_max3_f32 v60, v60, v61, v62
	s_waitcnt lgkmcnt(0)
	s_nop 1
	v_max_f32_dpp v60, v60, v60 quad_perm:[1,0,3,2] row_mask:0xf bank_mask:0xf
	s_nop 1
	v_max_f32_dpp v60, v60, v60 quad_perm:[2,3,0,1] row_mask:0xf bank_mask:0xf
	s_nop 1
	v_max_f32_dpp v60, v60, v60 row_half_mirror row_mask:0xf bank_mask:0xf
	s_nop 1
	v_max_f32_dpp v60, v60, v60 row_mirror row_mask:0xf bank_mask:0xf
	v_mov_b32_e32 v61, v60
	s_nop 1
	v_permlane16_swap_b32 v60, v61
	v_max_f32_e32 v60, v60, v61
	v_mov_b32_e32 v61, v60
	s_nop 1
	v_permlane32_swap_b32 v60, v61
	v_max_f32_e32 v60, v60, v61
	v_cmp_lt_f32_e32 vcc, 0, v60
	s_nop 1
	v_cndmask_b32_e32 v60, 1.0, v60, vcc
	s_and_saveexec_b64 s[20:21], s[4:5]
	s_cbranch_execz .LBB0_1558
	s_add_u32 s28, s8, s3
	s_addc_u32 s29, s9, s22
	v_mul_f32_e32 v61, 0x3c010204, v60
	global_store_dword v3, v61, s[28:29]
	s_branch .LBB0_1558

; __global__ void __launch_bounds__(NWAVES * 64, 2) fwd_kernel(Args a_unused) {
;     ...
;                 const float qi = 127.0f / am;
;                 if (lane == 0) ((float*)(ws + WS_CS + CS_ROW))[m] = am * (1.0f / 127.0f);
;                 unsigned* hq = (unsigned*)((signed char*)(ws + WS_H) + (size_t)m * D + 4 * lane);
; #pragma unroll
;                 for (int j = 0; j < 8; ++j) hq[64 * j] = q8x4(v[j][0], v[j][1], v[j][2], v[j][3], qi); }
;             f32x4 acc0 = {0.f, 0.f, 0.f, 0.f}, acc1 = {0.f, 0.f, 0.f, 0.f};
;             const unsigned short* xa = X1 + (size_t)(row0 + r16) * D + 256 * wave + 8 * kk;
; #pragma unroll
;             for (int sK = 0; sK < 8; ++sK) { const bf16x8 af = __builtin_bit_cast(bf16x8, *(const u32x4*)(xa + 32 * sK));
;                 acc0 = __builtin_amdgcn_mfma_f32_16x16x32_bf16(af, bh[sK][0], acc0, 0, 0, 0); acc0 = __builtin_amdgcn_mfma_f32_16x16x32_bf16(af, bl[sK][0], acc0, 0, 0, 0);
;                 acc1 = __builtin_amdgcn_mfma_f32_16x16x32_bf16(af, bh[sK][1], acc1, 0, 0, 0); acc1 = __builtin_amdgcn_mfma_f32_16x16x32_bf16(af, bl[sK][1], acc1, 0, 0, 0); }
; #pragma unroll
;             for (int q = 0; q < 4; ++q) { part[(wave * 16 + 4 * kk + q) * 32 + r16] = acc0[q]; part[(wave * 16 + 4 * kk + q) * 32 + 16 + r16] = acc1[q]; }
.LBB0_1871:
	s_or_b64 exec, exec, s[8:9]
	v_div_scale_f32 v198, s[8:9], v193, v193, s42
	v_rcp_f32_e32 v199, v198
	s_lshl_b64 s[6:7], s[6:7], 11
	v_fma_f32 v200, -v198, v199, 1.0
	v_fmac_f32_e32 v199, v200, v199
	v_div_scale_f32 v200, vcc, s42, v193, s42
	v_mul_f32_e32 v201, v200, v199
	v_fma_f32 v202, -v198, v201, v200
	v_fmac_f32_e32 v201, v202, v199
	v_fma_f32 v198, -v198, v201, v200
	v_div_fmas_f32 v198, v198, v199, v201
	v_div_fixup_f32 v193, v198, v193, s42
	v_fmaak_f32 v196, v196, v193, 0x4b400000
	v_fmaak_f32 v197, v197, v193, 0x4b400000
	v_fmaak_f32 v194, v194, v193, 0x4b400000
	v_fmaak_f32 v195, v195, v193, 0x4b400000
	v_perm_b32 v194, v195, v194, s43
	v_perm_b32 v195, v197, v196, s43
	v_lshl_add_u64 v[198:199], v[136:137], 0, s[6:7]
	v_perm_b32 v194, v194, v195, s44
	global_store_dword v[198:199], v194, off
	v_fmaak_f32 v194, v210, v193, 0x4b400000
	v_fmaak_f32 v195, v211, v193, 0x4b400000
	v_fmaak_f32 v196, v208, v193, 0x4b400000
	v_fmaak_f32 v197, v209, v193, 0x4b400000
	v_perm_b32 v196, v197, v196, s43
	v_perm_b32 v194, v195, v194, s43
	v_perm_b32 v194, v196, v194, s44
	global_store_dword v[198:199], v194, off offset:256
	v_fmaak_f32 v194, v214, v193, 0x4b400000
	v_fmaak_f32 v195, v215, v193, 0x4b400000
	v_fmaak_f32 v196, v212, v193, 0x4b400000
	v_fmaak_f32 v197, v213, v193, 0x4b400000
	v_perm_b32 v196, v197, v196, s43
	v_perm_b32 v194, v195, v194, s43
	v_perm_b32 v194, v196, v194, s44
	global_store_dword v[198:199], v194, off offset:512
	v_fmaak_f32 v194, v218, v193, 0x4b400000
	v_fmaak_f32 v195, v219, v193, 0x4b400000
	v_fmaak_f32 v196, v216, v193, 0x4b400000
	v_fmaak_f32 v197, v217, v193, 0x4b400000
	v_perm_b32 v196, v197, v196, s43
	v_perm_b32 v194, v195, v194, s43
	v_perm_b32 v194, v196, v194, s44
	global_store_dword v[198:199], v194, off offset:768
	v_fmaak_f32 v194, v222, v193, 0x4b400000
	v_fmaak_f32 v195, v223, v193, 0x4b400000
	v_fmaak_f32 v196, v220, v193, 0x4b400000
	v_fmaak_f32 v197, v221, v193, 0x4b400000
	v_perm_b32 v196, v197, v196, s43
	v_perm_b32 v194, v195, v194, s43
	v_perm_b32 v194, v196, v194, s44
	global_store_dword v[198:199], v194, off offset:1024
	v_fmaak_f32 v194, v226, v193, 0x4b400000
	v_fmaak_f32 v195, v227, v193, 0x4b400000
	v_fmaak_f32 v196, v224, v193, 0x4b400000
	v_fmaak_f32 v197, v225, v193, 0x4b400000
	v_fmaak_f32 v132, v132, v193, 0x4b400000
	v_fmaak_f32 v133, v133, v193, 0x4b400000
	v_fmaak_f32 v130, v130, v193, 0x4b400000
	v_fmaak_f32 v131, v131, v193, 0x4b400000
	v_perm_b32 v196, v197, v196, s43
	v_perm_b32 v194, v195, v194, s43
	v_perm_b32 v130, v131, v130, s43
	v_perm_b32 v131, v133, v132, s43
	v_perm_b32 v194, v196, v194, s44
	v_perm_b32 v130, v130, v131, s44
	global_store_dword v[198:199], v194, off offset:1280
	v_fmaak_f32 v194, v230, v193, 0x4b400000
	v_fmaak_f32 v195, v231, v193, 0x4b400000
	v_fmaak_f32 v196, v228, v193, 0x4b400000
	v_fmaak_f32 v197, v229, v193, 0x4b400000
	global_store_dword v[198:199], v130, off offset:1792
	v_add_u32_e32 v130, s36, v1
	v_perm_b32 v196, v197, v196, s43
	v_perm_b32 v194, v195, v194, s43
	v_ashrrev_i32_e32 v131, 31, v130
	v_perm_b32 v194, v196, v194, s44
	v_lshlrev_b64 v[130:131], 12, v[130:131]
	global_store_dword v[198:199], v194, off offset:1536
	v_lshl_add_u64 v[208:209], v[138:139], 0, v[130:131]
	global_load_dwordx4 v[130:133], v[208:209], off
	global_load_dwordx4 v[194:197], v[208:209], off offset:64
	global_load_dwordx4 v[210:213], v[208:209], off offset:128
	global_load_dwordx4 v[214:217], v[208:209], off offset:192
	global_load_dwordx4 v[218:221], v[208:209], off offset:256
	global_load_dwordx4 v[222:225], v[208:209], off offset:320
	global_load_dwordx4 v[226:229], v[208:209], off offset:384
	global_load_dwordx4 v[242:245], v[208:209], off offset:448
	s_waitcnt vmcnt(7)
	v_mfma_f32_16x16x32_bf16 v[198:201], v[130:133], v[122:125], 0
	v_mfma_f32_16x16x32_bf16 v[202:205], v[130:133], v[114:117], 0
	v_mfma_f32_16x16x32_bf16 v[198:201], v[130:133], v[126:129], v[198:201]
	v_mfma_f32_16x16x32_bf16 v[202:205], v[130:133], v[118:121], v[202:205]
	s_waitcnt vmcnt(6)
	v_mfma_f32_16x16x32_bf16 v[198:201], v[194:197], v[106:109], v[198:201]
	v_mfma_f32_16x16x32_bf16 v[202:205], v[194:197], v[98:101], v[202:205]
	v_mfma_f32_16x16x32_bf16 v[198:201], v[194:197], v[110:113], v[198:201]
	v_mfma_f32_16x16x32_bf16 v[202:205], v[194:197], v[102:105], v[202:205]
	s_waitcnt vmcnt(5)
	v_mfma_f32_16x16x32_bf16 v[198:201], v[210:213], v[90:93], v[198:201]
	v_mfma_f32_16x16x32_bf16 v[202:205], v[210:213], v[82:85], v[202:205]
	v_mfma_f32_16x16x32_bf16 v[198:201], v[210:213], v[94:97], v[198:201]
	v_mfma_f32_16x16x32_bf16 v[202:205], v[210:213], v[86:89], v[202:205]
	s_waitcnt vmcnt(4)
	v_mfma_f32_16x16x32_bf16 v[198:201], v[214:217], v[74:77], v[198:201]
	v_mfma_f32_16x16x32_bf16 v[202:205], v[214:217], v[66:69], v[202:205]
	v_mfma_f32_16x16x32_bf16 v[198:201], v[214:217], v[78:81], v[198:201]
	v_mfma_f32_16x16x32_bf16 v[202:205], v[214:217], v[70:73], v[202:205]
	s_waitcnt vmcnt(3)
	v_mfma_f32_16x16x32_bf16 v[198:201], v[218:221], v[58:61], v[198:201]
	v_mfma_f32_16x16x32_bf16 v[202:205], v[218:221], v[50:53], v[202:205]
	v_mfma_f32_16x16x32_bf16 v[198:201], v[218:221], v[62:65], v[198:201]
	v_mfma_f32_16x16x32_bf16 v[202:205], v[218:221], v[54:57], v[202:205]
	s_waitcnt vmcnt(2)
	v_mfma_f32_16x16x32_bf16 v[198:201], v[222:225], v[42:45], v[198:201]
	v_mfma_f32_16x16x32_bf16 v[202:205], v[222:225], v[34:37], v[202:205]
	v_mfma_f32_16x16x32_bf16 v[198:201], v[222:225], v[46:49], v[198:201]
	v_mfma_f32_16x16x32_bf16 v[202:205], v[222:225], v[38:41], v[202:205]
	s_waitcnt vmcnt(1)
	v_mfma_f32_16x16x32_bf16 v[198:201], v[226:229], v[26:29], v[198:201]
	v_mfma_f32_16x16x32_bf16 v[202:205], v[226:229], v[18:21], v[202:205]
	v_mfma_f32_16x16x32_bf16 v[198:201], v[226:229], v[30:33], v[198:201]
	v_mfma_f32_16x16x32_bf16 v[202:205], v[226:229], v[22:25], v[202:205]
	s_waitcnt vmcnt(0)
	v_mfma_f32_16x16x32_bf16 v[198:201], v[242:245], v[6:9], v[198:201]
	v_mfma_f32_16x16x32_bf16 v[202:205], v[242:245], v[2:5], v[202:205]
	v_mfma_f32_16x16x32_bf16 v[198:201], v[242:245], v[14:17], v[198:201]
	v_mfma_f32_16x16x32_bf16 v[202:205], v[242:245], v[10:13], v[202:205]
	s_nop 7
	ds_write2_b32 v239, v198, v202 offset1:16
	ds_write2_b32 v239, v199, v203 offset0:32 offset1:48
	ds_write2_b32 v239, v200, v204 offset0:64 offset1:80
	ds_write2_b32 v239, v201, v205 offset0:96 offset1:112
	s_waitcnt lgkmcnt(0)
	s_barrier
; __global__ void __launch_bounds__(NWAVES * 64, 2) fwd_kernel(Args a_unused) {
;     ...
;             { const int row = tid >> 5, e = tid & 31; float s = 0.f;
; #pragma unroll
;               for (int w = 0; w < 8; ++w) s += part[(w * 16 + row) * 32 + e];
;               float val = rsd[row] * s + cvec[e];
;               float tv[4]; int ti[4];
; #pragma unroll
;               for (int j = 0; j < 4; ++j) { float bv = val; int bi = e;
; #pragma unroll
;                   for (int off = 16; off >= 1; off >>= 1) { const float ov = __shfl_xor(bv, off); const int oi = __shfl_xor(bi, off); if (ov > bv || (ov == bv && oi < bi)) { bv = ov; bi = oi; } }
;                   tv[j] = bv; ti[j] = bi; if (e == bi) val = -INFINITY; }
	global_load_dword v131, v[140:141], off
	ds_read2st64_b32 v[132:133], v236 offset1:8
	ds_read2st64_b32 v[194:195], v236 offset0:16 offset1:24
	ds_read2st64_b32 v[196:197], v236 offset0:32 offset1:40
	ds_read2st64_b32 v[198:199], v236 offset0:48 offset1:56
	ds_read_b32 v130, v237 offset:16384
	s_waitcnt lgkmcnt(4)
	v_add_f32_e32 v132, 0, v132
	v_add_f32_e32 v132, v132, v133
	s_waitcnt lgkmcnt(3)
	v_add_f32_e32 v132, v132, v194
	v_add_f32_e32 v132, v132, v195
	s_waitcnt lgkmcnt(2)
	v_add_f32_e32 v132, v132, v196
	v_add_f32_e32 v132, v132, v197
	s_waitcnt lgkmcnt(1)
	v_add_f32_e32 v132, v132, v198
	v_add_f32_e32 v132, v132, v199
	ds_bpermute_b32 v194, v233, v235
	s_waitcnt vmcnt(0) lgkmcnt(1)
	v_fmac_f32_e32 v131, v132, v130
	ds_bpermute_b32 v193, v233, v131
	s_waitcnt lgkmcnt(0)
	v_cmp_lt_f32_e64 s[8:9], v131, v193
	v_cmp_nlt_f32_e32 vcc, v131, v193
	s_and_saveexec_b64 s[10:11], vcc
	v_cmp_eq_f32_e32 vcc, v131, v193
	v_cmp_lt_i32_e64 s[6:7], v194, v235
	s_and_b64 s[6:7], vcc, s[6:7]
	s_andn2_b64 s[8:9], s[8:9], exec
	s_and_b64 s[6:7], s[6:7], exec
	s_or_b64 s[8:9], s[8:9], s[6:7]
	s_or_b64 exec, exec, s[10:11]
	v_mov_b32_e32 v133, v131
	v_mov_b32_e32 v130, v131
	v_mov_b32_e32 v132, v235
	s_and_saveexec_b64 s[6:7], s[8:9]
	v_mov_b32_e32 v133, v193
	v_mov_b32_e32 v130, v193
	v_mov_b32_e32 v132, v194
	s_or_b64 exec, exec, s[6:7]
	ds_bpermute_b32 v193, v232, v133
	ds_bpermute_b32 v194, v232, v132
	s_waitcnt lgkmcnt(1)
	v_cmp_lt_f32_e64 s[8:9], v130, v193
	v_cmp_nlt_f32_e32 vcc, v130, v193
	s_and_saveexec_b64 s[10:11], vcc
	s_cbranch_execz .LBB0_1877
	v_cmp_eq_f32_e32 vcc, v130, v193
	s_waitcnt lgkmcnt(0)
	v_cmp_lt_i32_e64 s[6:7], v194, v132
	s_and_b64 s[6:7], vcc, s[6:7]
	s_andn2_b64 s[8:9], s[8:9], exec
	s_and_b64 s[6:7], s[6:7], exec
	s_or_b64 s[8:9], s[8:9], s[6:7]

; __global__ void __launch_bounds__(NWAVES * 64, 2) fwd_kernel(Args a_unused) {
;     ...
;         const int ntiles = *ntiles_p;
;         { const int nrows = ntiles * 256; unsigned v[8], vn[8]; const unsigned char* AF = (const unsigned char*)(ws + WS_ACT);
;           if (gw < nrows) { const unsigned char* ar = AF + (size_t)gw * FF + 4 * lane;
; #pragma unroll
;               for (int j = 0; j < 8; ++j) v[j] = *(const unsigned*)(ar + 256 * j); }
;           for (int m = gw; m < nrows; m += NGW) {
;               if (m + NGW < nrows) { const unsigned char* an = AF + (size_t)(m + NGW) * FF + 4 * lane;
; #pragma unroll
;                   for (int j = 0; j < 8; ++j) vn[j] = *(const unsigned*)(an + 256 * j); }
;               float f[8][4]; float am = 0.f;
; #pragma unroll
;               for (int j = 0; j < 8; ++j) { f[j][0] = __builtin_amdgcn_cvt_f32_fp8((int)v[j], 0); f[j][1] = __builtin_amdgcn_cvt_f32_fp8((int)v[j], 1); f[j][2] = __builtin_amdgcn_cvt_f32_fp8((int)v[j], 2); f[j][3] = __builtin_amdgcn_cvt_f32_fp8((int)v[j], 3);
;                   am = fmaxf(am, fmaxf(fmaxf(fabsf(f[j][0]), fabsf(f[j][1])), fmaxf(fabsf(f[j][2]), fabsf(f[j][3])))); }
; #pragma unroll
;               for (int o = 1; o < 64; o <<= 1) am = fmaxf(am, __shfl_xor(am, o));
;               if (!(am > 0.f)) am = 1.f;
;               const float qi = 127.0f / am;
;               if (lane == 0) ((float*)(ws + WS_ROUTE + RT_ARS))[m] = am * (1.0f / 127.0f);
;               unsigned* aq = (unsigned*)((signed char*)(ws + WS_ACT8) + (size_t)m * FF + 4 * lane);
; #pragma unroll
;               for (int j = 0; j < 8; ++j) { const unsigned b0 = __float_as_uint(__builtin_fmaf(f[j][0], qi, 12582912.0f)), b1 = __float_as_uint(__builtin_fmaf(f[j][1], qi, 12582912.0f)),
;                                                            b2 = __float_as_uint(__builtin_fmaf(f[j][2], qi, 12582912.0f)), b3 = __float_as_uint(__builtin_fmaf(f[j][3], qi, 12582912.0f));
;                   aq[64 * j] = __builtin_amdgcn_perm(__builtin_amdgcn_perm(b3, b2, 0x0c0c0400u), __builtin_amdgcn_perm(b1, b0, 0x0c0c0400u), 0x05040100u); }
; #pragma unroll
;               for (int j = 0; j < 8; ++j) v[j] = vn[j];
.LBB0_2347:
	s_cmp_lt_i32 s46, 12
	s_cselect_b64 s[6:7], -1, 0
	s_and_b64 s[10:11], s[6:7], s[4:5]
	s_andn2_b64 vcc, exec, s[10:11]
	s_cbranch_vccnz .LBB0_2492
	s_mov_b64 s[6:7], s[78:79]
	s_load_dwordx2 s[12:13], s[6:7], 0xc8
	v_mov_b32_e32 v1, 0x181000
	s_waitcnt lgkmcnt(0)
	global_load_dword v1, v1, s[12:13] offset:2048
	s_waitcnt vmcnt(0)
	v_readfirstlane_b32 s70, v1
	s_lshl_b32 s3, s70, 8
	s_cmp_ge_i32 s58, s3
	s_cbranch_scc1 .LBB0_2355
	s_ashr_i32 s59, s58, 31
	s_lshl_b64 s[8:9], s[58:59], 11
	s_add_u32 s4, s12, s8
	s_addc_u32 s5, s13, s9
	v_mov_b32_e32 v165, 0
	v_lshl_add_u64 v[2:3], s[4:5], 0, v[164:165]
	s_mov_b64 s[4:5], 0x3ae00000
	v_lshl_add_u64 v[4:5], v[2:3], 0, s[4:5]
	v_add_co_u32_e32 v2, vcc, 0x3ae00000, v2
	v_mbcnt_lo_u32_b32 v1, -1, 0
	s_nop 0
	v_addc_co_u32_e32 v3, vcc, 0, v3, vcc
	global_load_dword v26, v[2:3], off
	global_load_dword v25, v[4:5], off offset:256
	global_load_dword v24, v[4:5], off offset:512
	global_load_dword v23, v[4:5], off offset:768
	global_load_dword v22, v[4:5], off offset:1024
	global_load_dword v21, v[4:5], off offset:1280
	global_load_dword v20, v[4:5], off offset:1536
	global_load_dword v19, v[4:5], off offset:1792
	v_mbcnt_hi_u32_b32 v2, -1, v1
	v_and_b32_e32 v1, 64, v2
	v_add_u32_e32 v3, 64, v1
	v_xor_b32_e32 v1, 1, v2
	v_cmp_lt_i32_e32 vcc, v1, v3
	v_xor_b32_e32 v4, 2, v2
	s_ashr_i32 s57, s56, 31
	v_cndmask_b32_e32 v1, v2, v1, vcc
	v_cmp_lt_i32_e32 vcc, v4, v3
	s_lshl_b64 s[14:15], s[58:59], 2
	v_cmp_eq_u32_e64 s[4:5], 0, v162
	v_cndmask_b32_e32 v4, v2, v4, vcc
	v_lshlrev_b32_e32 v6, 2, v4
	v_xor_b32_e32 v4, 4, v2
	v_cmp_lt_i32_e32 vcc, v4, v3
	v_lshlrev_b32_e32 v1, 2, v1
	s_mov_b32 s22, 0x42fe0000
	v_cndmask_b32_e32 v4, v2, v4, vcc
	v_lshlrev_b32_e32 v7, 2, v4
	v_xor_b32_e32 v4, 8, v2
	v_cmp_lt_i32_e32 vcc, v4, v3
	s_mov_b32 s23, 0xc0c0400
	s_mov_b32 s24, 0x5040100
	v_cndmask_b32_e32 v4, v2, v4, vcc
	v_lshlrev_b32_e32 v8, 2, v4
	v_xor_b32_e32 v4, 16, v2
	v_cmp_lt_i32_e32 vcc, v4, v3
	s_mov_b32 s25, 0x4fc00000
	s_mov_b32 s26, s58
	v_cndmask_b32_e32 v4, v2, v4, vcc
	v_lshlrev_b32_e32 v9, 2, v4
	v_xor_b32_e32 v4, 32, v2
	v_cmp_lt_i32_e32 vcc, v4, v3
	v_mov_b32_e32 v3, s9
	s_nop 0
	v_cndmask_b32_e32 v2, v2, v4, vcc
	v_lshlrev_b32_e32 v10, 2, v2
	v_or_b32_e32 v2, s8, v164
	s_lshl_b64 s[8:9], s[56:57], 11
	s_add_u32 s20, s14, 0x390000
	s_addc_u32 s21, s15, 0
	s_add_i32 s16, s58, s56
	s_ashr_i32 s17, s16, 31
	s_lshl_b64 s[16:17], s[16:17], 11
	s_lshl_b64 s[14:15], s[56:57], 2
	v_or_b32_e32 v4, s16, v164
	v_mov_b32_e32 v5, s17
	s_waitcnt vmcnt(0)
	s_branch .LBB0_2351
.LBB0_2350:
	s_or_b64 exec, exec, s[18:19]
	v_div_scale_f32 v52, s[18:19], v51, v51, s22
	v_rcp_f32_e32 v53, v52
	v_div_scale_f32 v54, vcc, s22, v51, s22
	s_add_u32 s20, s20, s14
	v_fma_f32 v55, -v52, v53, 1.0
	v_fmac_f32_e32 v53, v55, v53
	v_mul_f32_e32 v55, v54, v53
	v_fma_f32 v56, -v52, v55, v54
	v_fmac_f32_e32 v55, v56, v53
	v_fma_f32 v52, -v52, v55, v54
	v_div_fmas_f32 v52, v52, v53, v55
	v_div_fixup_f32 v51, v52, v51, s22
	v_lshl_add_u64 v[52:53], s[12:13], 0, v[2:3]
	v_fmaak_f32 v32, v32, v51, 0x4b400000
	v_fmaak_f32 v33, v33, v51, 0x4b400000
	v_fmaak_f32 v29, v29, v51, 0x4b400000
	v_fmaak_f32 v27, v27, v51, 0x4b400000
	v_perm_b32 v27, v27, v29, s23
	v_perm_b32 v29, v33, v32, s23
	v_add_co_u32_e32 v32, vcc, s25, v52
	v_perm_b32 v27, v27, v29, s24
	s_nop 0
	v_addc_co_u32_e32 v33, vcc, 0, v53, vcc
	global_store_dword v[32:33], v27, off
	v_fmaak_f32 v27, v30, v51, 0x4b400000
	v_fmaak_f32 v29, v31, v51, 0x4b400000
	v_fmaak_f32 v28, v28, v51, 0x4b400000
	v_fmaak_f32 v26, v26, v51, 0x4b400000
	v_perm_b32 v26, v26, v28, s23
	v_perm_b32 v27, v29, v27, s23
	v_perm_b32 v26, v26, v27, s24
	global_store_dword v[32:33], v26, off offset:256
	v_fmaak_f32 v26, v35, v51, 0x4b400000
	v_fmaak_f32 v27, v36, v51, 0x4b400000
	v_fmaak_f32 v28, v34, v51, 0x4b400000
	v_fmaak_f32 v25, v25, v51, 0x4b400000
	v_perm_b32 v25, v25, v28, s23
	v_perm_b32 v26, v27, v26, s23
	v_perm_b32 v25, v25, v26, s24
	global_store_dword v[32:33], v25, off offset:512
	v_fmaak_f32 v25, v38, v51, 0x4b400000
	v_fmaak_f32 v26, v39, v51, 0x4b400000
	v_fmaak_f32 v27, v37, v51, 0x4b400000
	v_fmaak_f32 v24, v24, v51, 0x4b400000
	v_perm_b32 v24, v24, v27, s23
	v_perm_b32 v25, v26, v25, s23
	v_perm_b32 v24, v24, v25, s24
	global_store_dword v[32:33], v24, off offset:768
	v_fmaak_f32 v24, v41, v51, 0x4b400000
	v_fmaak_f32 v25, v42, v51, 0x4b400000
	v_fmaak_f32 v26, v40, v51, 0x4b400000
	v_fmaak_f32 v23, v23, v51, 0x4b400000
	v_perm_b32 v23, v23, v26, s23
	v_perm_b32 v24, v25, v24, s23
	v_perm_b32 v23, v23, v24, s24
	global_store_dword v[32:33], v23, off offset:1024
	v_fmaak_f32 v23, v44, v51, 0x4b400000
	v_fmaak_f32 v24, v45, v51, 0x4b400000
	v_fmaak_f32 v25, v43, v51, 0x4b400000
	v_fmaak_f32 v22, v22, v51, 0x4b400000
	v_perm_b32 v22, v22, v25, s23
	v_perm_b32 v23, v24, v23, s23
	v_perm_b32 v22, v22, v23, s24
	global_store_dword v[32:33], v22, off offset:1280
	v_fmaak_f32 v22, v47, v51, 0x4b400000
	v_fmaak_f32 v23, v48, v51, 0x4b400000
	v_fmaak_f32 v24, v46, v51, 0x4b400000
	v_fmaak_f32 v21, v21, v51, 0x4b400000
	v_perm_b32 v21, v21, v24, s23
	v_perm_b32 v22, v23, v22, s23
	v_perm_b32 v21, v21, v22, s24
	global_store_dword v[32:33], v21, off offset:1536
	v_fmaak_f32 v21, v50, v51, 0x4b400000
	v_fmaak_f32 v19, v19, v51, 0x4b400000
	v_fmaak_f32 v22, v49, v51, 0x4b400000
	v_fmaak_f32 v20, v20, v51, 0x4b400000
	v_perm_b32 v20, v20, v22, s23
	v_perm_b32 v19, v19, v21, s23
	v_perm_b32 v19, v20, v19, s24
	global_store_dword v[32:33], v19, off offset:1792
	v_lshl_add_u64 v[2:3], v[2:3], 0, s[8:9]
	s_addc_u32 s21, s21, s15
	v_lshl_add_u64 v[4:5], v[4:5], 0, s[8:9]
	s_and_b64 vcc, exec, s[16:17]
	s_waitcnt vmcnt(8)
	v_mov_b32_e32 v19, v11
	v_mov_b32_e32 v20, v12
	v_mov_b32_e32 v21, v13
	v_mov_b32_e32 v22, v14
	v_mov_b32_e32 v23, v15
	v_mov_b32_e32 v24, v16
	v_mov_b32_e32 v25, v17
	v_mov_b32_e32 v26, v18
	s_cbranch_vccnz .LBB0_2355

; __global__ void __launch_bounds__(NWAVES * 64, 2) fwd_kernel(Args a_unused) {
;     ...
;               float f[8][4]; float am = 0.f;
; #pragma unroll
;               for (int j = 0; j < 8; ++j) { f[j][0] = __builtin_amdgcn_cvt_f32_fp8((int)v[j], 0); f[j][1] = __builtin_amdgcn_cvt_f32_fp8((int)v[j], 1); f[j][2] = __builtin_amdgcn_cvt_f32_fp8((int)v[j], 2); f[j][3] = __builtin_amdgcn_cvt_f32_fp8((int)v[j], 3);
;                   am = fmaxf(am, fmaxf(fmaxf(fabsf(f[j][0]), fabsf(f[j][1])), fmaxf(fabsf(f[j][2]), fabsf(f[j][3])))); }
; #pragma unroll
;               for (int o = 1; o < 64; o <<= 1) am = fmaxf(am, __shfl_xor(am, o));
;               if (!(am > 0.f)) am = 1.f;
;               const float qi = 127.0f / am;
;               if (lane == 0) ((float*)(ws + WS_ROUTE + RT_ARS))[m] = am * (1.0f / 127.0f);
.LBB0_2353:
	v_cvt_f32_fp8_sdwa v27, v26 src0_sel:BYTE_3
	v_cvt_f32_fp8_sdwa v29, v26 src0_sel:BYTE_2
	v_cvt_f32_fp8_e32 v32, v26
	v_cvt_f32_fp8_sdwa v33, v26 src0_sel:BYTE_1
	v_max_f32_e64 v26, |v27|, |v27|
	v_max_f32_e64 v28, |v29|, |v29|
	v_max_f32_e32 v26, v28, v26
	v_max3_f32 v34, |v32|, |v33|, v26
	v_cvt_f32_fp8_sdwa v26, v25 src0_sel:BYTE_3
	v_cvt_f32_fp8_sdwa v28, v25 src0_sel:BYTE_2
	v_cvt_f32_fp8_e32 v30, v25
	v_cvt_f32_fp8_sdwa v31, v25 src0_sel:BYTE_1
	v_max_f32_e64 v25, |v26|, |v26|
	v_max_f32_e64 v35, |v28|, |v28|
	v_max_f32_e32 v25, v35, v25
	v_max3_f32 v25, |v30|, |v31|, v25
	v_max3_f32 v40, v34, 0, v25
	v_cvt_f32_fp8_sdwa v25, v24 src0_sel:BYTE_3
	v_cvt_f32_fp8_sdwa v34, v24 src0_sel:BYTE_2
	v_cvt_f32_fp8_e32 v35, v24
	v_cvt_f32_fp8_sdwa v36, v24 src0_sel:BYTE_1
	v_max_f32_e64 v24, |v25|, |v25|
	v_max_f32_e64 v37, |v34|, |v34|
	v_max_f32_e32 v24, v37, v24
	v_max3_f32 v41, |v35|, |v36|, v24
	v_cvt_f32_fp8_sdwa v24, v23 src0_sel:BYTE_3
	v_cvt_f32_fp8_sdwa v37, v23 src0_sel:BYTE_2
	v_cvt_f32_fp8_e32 v38, v23
	v_cvt_f32_fp8_sdwa v39, v23 src0_sel:BYTE_1
	v_max_f32_e64 v23, |v24|, |v24|
	v_max_f32_e64 v42, |v37|, |v37|
	v_max_f32_e32 v23, v42, v23
	v_max3_f32 v23, |v38|, |v39|, v23
	v_max3_f32 v46, v40, v41, v23
	v_cvt_f32_fp8_sdwa v23, v22 src0_sel:BYTE_3
	v_cvt_f32_fp8_sdwa v40, v22 src0_sel:BYTE_2
	v_cvt_f32_fp8_e32 v41, v22
	v_cvt_f32_fp8_sdwa v42, v22 src0_sel:BYTE_1
	v_max_f32_e64 v22, |v23|, |v23|
	v_max_f32_e64 v43, |v40|, |v40|
	v_max_f32_e32 v22, v43, v22
	v_max3_f32 v47, |v41|, |v42|, v22
	v_cvt_f32_fp8_sdwa v22, v21 src0_sel:BYTE_3
	v_cvt_f32_fp8_sdwa v43, v21 src0_sel:BYTE_2
	v_cvt_f32_fp8_e32 v44, v21
	v_cvt_f32_fp8_sdwa v45, v21 src0_sel:BYTE_1
	v_max_f32_e64 v21, |v22|, |v22|
	v_max_f32_e64 v48, |v43|, |v43|
	v_max_f32_e32 v21, v48, v21
	v_max3_f32 v21, |v44|, |v45|, v21
	v_max3_f32 v51, v46, v47, v21
	v_cvt_f32_fp8_sdwa v21, v20 src0_sel:BYTE_3
	v_cvt_f32_fp8_sdwa v46, v20 src0_sel:BYTE_2
	v_cvt_f32_fp8_e32 v47, v20
	v_cvt_f32_fp8_sdwa v48, v20 src0_sel:BYTE_1
	v_max_f32_e64 v20, |v21|, |v21|
	v_max_f32_e64 v49, |v46|, |v46|
	v_max_f32_e32 v20, v49, v20
	v_max3_f32 v52, |v47|, |v48|, v20
	v_cvt_f32_fp8_sdwa v20, v19 src0_sel:BYTE_3
	v_cvt_f32_fp8_sdwa v49, v19 src0_sel:BYTE_2
	v_cvt_f32_fp8_e32 v50, v19
	v_cvt_f32_fp8_sdwa v19, v19 src0_sel:BYTE_1
	v_max_f32_e64 v53, |v20|, |v20|
	v_max_f32_e64 v54, |v49|, |v49|
	v_max_f32_e32 v53, v54, v53
	v_max3_f32 v53, |v50|, |v19|, v53
	v_max3_f32 v51, v51, v52, v53
	s_waitcnt lgkmcnt(0)
	s_nop 1
	v_max_f32_dpp v51, v51, v51 quad_perm:[1,0,3,2] row_mask:0xf bank_mask:0xf
	s_nop 1
	v_max_f32_dpp v51, v51, v51 quad_perm:[2,3,0,1] row_mask:0xf bank_mask:0xf
	s_nop 1
	v_max_f32_dpp v51, v51, v51 row_half_mirror row_mask:0xf bank_mask:0xf
	s_nop 1
	v_max_f32_dpp v51, v51, v51 row_mirror row_mask:0xf bank_mask:0xf
	v_mov_b32_e32 v52, v51
	s_nop 1
	v_permlane16_swap_b32 v51, v52
	v_max_f32_e32 v51, v51, v52
	v_mov_b32_e32 v52, v51
	s_nop 1
	v_permlane32_swap_b32 v51, v52
	v_max_f32_e32 v51, v51, v52
	v_cmp_lt_f32_e32 vcc, 0, v51
	s_nop 1
	v_cndmask_b32_e32 v51, 1.0, v51, vcc
	s_and_saveexec_b64 s[18:19], s[4:5]
	s_cbranch_execz .LBB0_2350
	s_add_u32 s28, s12, s20
	s_addc_u32 s29, s13, s21
	v_mul_f32_e32 v52, 0x3c010204, v51
	global_store_dword v165, v52, s[28:29]
	s_branch .LBB0_2350
